# attn: exp rebalance + rowmax hidden under PV MFMAs + younger-half prio in PV phase; nops removed
# speedup vs baseline: 1.0057x; 1.0057x over previous
_ZN3att8attn_fwdEPKDF16_PDF16_:
	s_load_dwordx4 s[4:7], s[0:1], 0x0
	s_lshl_b32 s0, s2, 2
	s_and_b32 s0, s0, 28
	s_lshr_b32 s1, s2, 6
	v_readfirstlane_b32 s10, v0
	s_add_i32 s8, s0, s1
	s_lshl_b32 s0, s2, 5
	s_mov_b32 s9, 0
	s_lshr_b32 s26, s10, 6
	s_and_b32 s27, s0, 0x700
	s_lshl_b64 s[0:1], s[8:9], 11
	s_or_b32 s0, s0, s27
	s_lshl_b32 s28, s26, 5
	s_add_u32 s0, s0, s28
	s_addc_u32 s1, s1, 0
	s_lshl_b64 s[0:1], s[0:1], 7
	s_waitcnt lgkmcnt(0)
	s_add_u32 s12, s4, s0
	s_addc_u32 s13, s5, s1
	s_lshl_b64 s[2:3], s[8:9], 18
	s_add_u32 s1, s4, s2
	s_addc_u32 s15, s5, s3
	s_and_b32 s0, s10, 0x3fffffc0
	s_lshl_b32 s10, s26, 9
	s_mov_b32 s11, s9
	s_lshl_b64 s[10:11], s[10:11], 1
	v_and_b32_e32 v190, 63, v0
	s_add_u32 s14, s1, s10
	s_addc_u32 s15, s15, s11
	v_lshlrev_b32_e32 v184, 4, v190
	v_mov_b32_e32 v185, 0
	v_lshl_add_u64 v[48:49], s[14:15], 0, v[184:185]
	s_mov_b64 s[14:15], 0x800000
	s_lshl_b32 s1, s26, 10
	v_lshl_add_u64 v[180:181], v[48:49], 0, s[14:15]
	s_mov_b64 s[14:15], 0x1000000
	s_cmp_lg_u32 0, -1
	v_lshl_add_u64 v[182:183], v[48:49], 0, s[14:15]
	s_cselect_b32 s14, 0, 0
	v_bfe_u32 v192, v0, 5, 1
	s_add_i32 s30, s1, s14
	s_mov_b32 s1, m0
	s_mov_b32 m0, s30
	s_nop 0
	global_load_lds_dwordx4 v[180:181], off
	s_mov_b32 m0, s1
	v_and_b32_e32 v191, 31, v0
	s_add_i32 s31, s30, 0x6000
	s_mov_b32 s1, m0
	s_mov_b32 m0, s31
	s_nop 0
	global_load_lds_dwordx4 v[182:183], off
	s_mov_b32 m0, s1
	s_mov_b64 s[14:15], 0x802000
	v_lshlrev_b32_e32 v195, 4, v192
	v_lshl_add_u64 v[2:3], v[48:49], 0, s[14:15]
	s_add_i32 s1, s30, 0x2000
	s_mov_b32 s14, m0
	s_mov_b32 m0, s1
	s_nop 0
	global_load_lds_dwordx4 v[2:3], off
	s_mov_b32 m0, s14
	v_lshl_or_b32 v1, v191, 7, v195
	global_load_dwordx4 v[136:139], v1, s[12:13]
	global_load_dwordx4 v[128:131], v1, s[12:13] offset:32
	global_load_dwordx4 v[120:123], v1, s[12:13] offset:64
	global_load_dwordx4 v[116:119], v1, s[12:13] offset:96
	s_mov_b64 s[14:15], 0x804000
	v_mov_b32_e32 v2, v185
	v_mov_b32_e32 v3, v185
	v_mov_b32_e32 v4, v185
	v_mov_b32_e32 v5, v185
	v_mov_b32_e32 v6, v185
	v_mov_b32_e32 v7, v185
	v_mov_b32_e32 v8, v185
	v_mov_b32_e32 v9, v185
	v_mov_b32_e32 v10, v185
	v_mov_b32_e32 v11, v185
	v_mov_b32_e32 v12, v185
	v_mov_b32_e32 v13, v185
	v_mov_b32_e32 v14, v185
	v_mov_b32_e32 v15, v185
	v_mov_b32_e32 v16, v185
	v_mov_b32_e32 v17, v185
	v_lshlrev_b32_e32 v1, 10, v192
	v_lshlrev_b32_e32 v18, 4, v191
	v_add3_u32 v198, 0, v1, v18
	v_lshl_add_u64 v[18:19], v[48:49], 0, s[14:15]
	s_add_i32 s1, s30, 0x4000
	s_mov_b32 s12, m0
	s_mov_b32 m0, s1
	s_nop 0
	global_load_lds_dwordx4 v[18:19], off
	s_mov_b32 m0, s12
	s_waitcnt vmcnt(3) lgkmcnt(0)
	s_barrier
	ds_read_b128 v[34:37], v198
	ds_read_b128 v[38:41], v198 offset:512
	v_lshlrev_b32_e32 v193, 3, v0
	s_mov_b64 s[16:17], 0x1002000
	s_add_i32 s1, s30, 0x8000
	s_lshl_b32 s0, s0, 2
	s_add_i32 s29, s0, 0
	s_add_u32 s2, s10, s2
	s_addc_u32 s3, s11, s3
	s_mov_b32 s20, -1
	s_movk_i32 s23, 0x2000
	s_movk_i32 s21, 0x4000
	s_mov_b64 s[10:11], 0x2000
	s_mov_b32 s22, 0x41000000
	s_mov_b64 s[14:15], 0x4000
	v_lshl_add_u32 v196, v191, 2, s29
	v_mov_b32_e32 v199, 0
	s_waitcnt vmcnt(3) lgkmcnt(1)
	v_mfma_f32_32x32x16_f16 v[18:33], v[34:37], v[136:139], v[2:17]
	s_waitcnt lgkmcnt(0)
	v_mfma_f32_32x32x16_f16 v[2:17], v[38:41], v[136:139], v[2:17]
	ds_read_b128 v[34:37], v198 offset:2048
	ds_read_b128 v[38:41], v198 offset:2560
	s_waitcnt vmcnt(2) lgkmcnt(1)
	v_mfma_f32_32x32x16_f16 v[18:33], v[34:37], v[128:131], v[18:33]
	s_waitcnt lgkmcnt(0)
	v_mfma_f32_32x32x16_f16 v[2:17], v[38:41], v[128:131], v[2:17]
	ds_read_b128 v[34:37], v198 offset:4096
	ds_read_b128 v[38:41], v198 offset:4608
	s_waitcnt vmcnt(1) lgkmcnt(1)
	v_mfma_f32_32x32x16_f16 v[18:33], v[34:37], v[120:123], v[18:33]
	s_waitcnt lgkmcnt(0)
	v_mfma_f32_32x32x16_f16 v[2:17], v[38:41], v[120:123], v[2:17]
	ds_read_b128 v[34:37], v198 offset:6144
	ds_read_b128 v[38:41], v198 offset:6656
	s_waitcnt vmcnt(0) lgkmcnt(1)
	v_mfma_f32_32x32x16_f16 v[18:33], v[34:37], v[116:119], v[18:33]
	s_waitcnt lgkmcnt(0)
	v_mfma_f32_32x32x16_f16 v[2:17], v[38:41], v[116:119], v[2:17]
	s_nop 9
	v_max_f32_e32 v1, v19, v19
	v_max_f32_e32 v34, v18, v18
	v_max_f32_e32 v1, v34, v1
	v_max3_f32 v35, v20, v21, v3
	v_max3_f32 v1, v1, v2, v4
	v_max3_f32 v34, v35, v24, v25
	v_max3_f32 v1, v1, v5, v22
	v_max3_f32 v34, v34, v8, v9
	v_max3_f32 v1, v1, v23, v6
	v_max3_f32 v34, v34, v28, v29
	v_max3_f32 v1, v1, v7, v26
	v_max3_f32 v34, v34, v12, v13
	v_max3_f32 v1, v1, v27, v10
	v_max3_f32 v34, v34, v32, v33
	v_max3_f32 v1, v1, v11, v30
	v_max3_f32 v34, v34, v16, v17
	v_max3_f32 v1, v1, v31, v14
	v_max3_f32 v1, v1, v15, v34
	v_mov_b32_e32 v34, v1
	s_nop 1
	v_permlane32_swap_b32_e32 v1, v34
	v_max_f32_e32 v34, v34, v34
	v_max_f32_e32 v1, v1, v1
	v_max_f32_e32 v197, v1, v34
	v_lshlrev_b32_e32 v1, 1, v0
	v_sub_f32_e32 v62, v32, v197
	v_and_b32_e32 v1, 32, v1
	v_and_b32_e32 v32, 24, v193
	v_lshlrev_b32_e32 v0, 4, v0
	v_add3_u32 v1, 0, v1, v32
	v_and_b32_e32 v0, 0xc0, v0
	v_lshlrev_b32_e32 v32, 8, v192
	v_add3_u32 v194, v1, v32, v0
	v_xor_b32_e32 v32, 0x80000000, v197
	v_sub_f32_e32 v63, v33, v197
	v_mov_b32_e32 v33, v32
	v_mov_b32_e32 v34, v32
	v_mov_b32_e32 v35, v32
	v_mov_b32_e32 v36, v32
	v_mov_b32_e32 v37, v32
	v_mov_b32_e32 v38, v32
	v_mov_b32_e32 v39, v32
	v_mov_b32_e32 v40, v32
	v_mov_b32_e32 v41, v32
	v_mov_b32_e32 v42, v32
	v_mov_b32_e32 v43, v32
	v_mov_b32_e32 v44, v32
	v_mov_b32_e32 v45, v32
	v_mov_b32_e32 v46, v32
	v_mov_b32_e32 v47, v32
	s_waitcnt vmcnt(0) lgkmcnt(0)
	s_barrier
	v_lshl_add_u64 v[0:1], v[48:49], 0, s[16:17]
	s_mov_b32 s12, m0
	s_mov_b32 m0, s1
	s_nop 0
	global_load_lds_dwordx4 v[0:1], off
	s_mov_b32 m0, s12
	s_mov_b64 s[12:13], 0x806000
	v_lshl_add_u64 v[0:1], v[48:49], 0, s[12:13]
	s_mov_b32 s1, m0
	s_mov_b32 m0, s30
	s_nop 0
	global_load_lds_dwordx4 v[0:1], off
	s_mov_b32 m0, s1
	ds_read_b128 v[172:175], v198 offset:8192
	ds_read_b128 v[168:171], v198 offset:8704
	ds_read_b128 v[164:167], v198 offset:10240
	ds_read_b128 v[160:163], v198 offset:10752
	ds_read_b128 v[156:159], v198 offset:12288
	ds_read_b128 v[152:155], v198 offset:12800
	ds_read_b128 v[148:151], v198 offset:14336
	ds_read_b128 v[144:147], v198 offset:14848
	v_sub_f32_e32 v18, v18, v197
	v_sub_f32_e32 v19, v19, v197
	v_sub_f32_e32 v20, v20, v197
	v_sub_f32_e32 v21, v21, v197
	v_sub_f32_e32 v22, v22, v197
	v_sub_f32_e32 v23, v23, v197
	v_sub_f32_e32 v24, v24, v197
	v_sub_f32_e32 v25, v25, v197
	v_sub_f32_e32 v26, v26, v197
	v_sub_f32_e32 v27, v27, v197
	v_sub_f32_e32 v28, v28, v197
	v_sub_f32_e32 v29, v29, v197
	v_sub_f32_e32 v30, v30, v197
	v_sub_f32_e32 v31, v31, v197
	v_sub_f32_e32 v2, v2, v197
	v_sub_f32_e32 v3, v3, v197
	v_sub_f32_e32 v4, v4, v197
	v_sub_f32_e32 v5, v5, v197
	v_sub_f32_e32 v6, v6, v197
	v_sub_f32_e32 v7, v7, v197
	v_sub_f32_e32 v8, v8, v197
	v_sub_f32_e32 v9, v9, v197
	v_sub_f32_e32 v10, v10, v197
	v_sub_f32_e32 v11, v11, v197
	v_sub_f32_e32 v12, v12, v197
	v_sub_f32_e32 v13, v13, v197
	v_sub_f32_e32 v14, v14, v197
	v_sub_f32_e32 v15, v15, v197
	v_sub_f32_e32 v16, v16, v197
	v_sub_f32_e32 v17, v17, v197
	v_exp_f32_e32 v64, v18
	v_exp_f32_e32 v65, v19
	v_exp_f32_e32 v48, v2
	v_exp_f32_e32 v49, v3
	v_exp_f32_e32 v66, v20
	v_exp_f32_e32 v50, v4
	v_mov_b32_e32 v67, v21
	v_mov_b32_e32 v51, v5
	v_exp_f32_e32 v68, v22
	v_exp_f32_e32 v52, v6
	v_exp_f32_e32 v69, v23
	v_exp_f32_e32 v53, v7
	v_exp_f32_e32 v70, v24
	v_exp_f32_e32 v54, v8
	v_mov_b32_e32 v71, v25
	v_mov_b32_e32 v55, v9
	v_exp_f32_e32 v72, v26
	v_exp_f32_e32 v56, v10
	v_exp_f32_e32 v73, v27
	v_exp_f32_e32 v57, v11
	v_exp_f32_e32 v74, v28
	v_exp_f32_e32 v58, v12
	v_mov_b32_e32 v75, v29
	v_mov_b32_e32 v59, v13
	v_exp_f32_e32 v76, v30
	v_exp_f32_e32 v60, v14
	v_exp_f32_e32 v77, v31
	v_exp_f32_e32 v61, v15
	v_exp_f32_e32 v78, v62
	v_exp_f32_e32 v62, v16
	v_mov_b32_e32 v79, v63
	v_mov_b32_e32 v63, v17
	s_waitcnt vmcnt(2) lgkmcnt(0)
	s_barrier
	v_or_b32_e32 v0, s2, v184
	v_mov_b32_e32 v1, s3
	v_lshl_add_u64 v[186:187], s[4:5], 0, v[0:1]
	s_mov_b32 s2, 0xff800000
	s_mov_b32 s4, 0xff806000
	v_cmp_gt_u32_e64 s[0:1], 32, v190
	s_mov_b32 s3, -1
	s_mov_b32 s5, -1
	s_mov_b64 s[12:13], 0x8000
	v_mov_b32_e32 v0, 0
	v_mov_b32_e32 v1, v185
	v_mov_b32_e32 v2, v185
	v_mov_b32_e32 v3, v185
	v_mov_b32_e32 v4, v185
	v_mov_b32_e32 v5, v185
	v_mov_b32_e32 v6, v185
	v_mov_b32_e32 v7, v185
	v_mov_b32_e32 v8, v185
	v_mov_b32_e32 v9, v185
	v_mov_b32_e32 v10, v185
	v_mov_b32_e32 v11, v185
	v_mov_b32_e32 v12, v185
	v_mov_b32_e32 v13, v185
	v_mov_b32_e32 v14, v185
	v_mov_b32_e32 v15, v185
	v_mov_b32_e32 v16, 0
	v_mov_b32_e32 v17, v185
	v_mov_b32_e32 v18, v185
	v_mov_b32_e32 v19, v185
	v_mov_b32_e32 v20, v185
	v_mov_b32_e32 v21, v185
	v_mov_b32_e32 v22, v185
	v_mov_b32_e32 v23, v185
	v_mov_b32_e32 v24, v185
	v_mov_b32_e32 v25, v185
	v_mov_b32_e32 v26, v185
	v_mov_b32_e32 v27, v185
	v_mov_b32_e32 v28, v185
	v_mov_b32_e32 v29, v185
	v_mov_b32_e32 v30, v185
	v_mov_b32_e32 v31, v185
	v_lshl_add_u64 v[188:189], v[186:187], 0, s[16:17]
.LBB3_1:
	v_add_u32_e32 v184, s9, v194
	ds_read_b64_tr_b16 v[176:177], v184 offset:24576
	ds_read_b64_tr_b16 v[178:179], v184 offset:25088
	s_waitcnt lgkmcnt(9)
	v_mfma_f32_32x32x16_f16 v[96:111], v[172:175], v[136:139], v[32:47]
	v_exp_f32_e32 v67, v67
	v_cvt_pk_f16_f32 v140, v64, v65
	v_cvt_pk_f16_f32 v141, v66, v67
	v_pk_add_f16 v64, v185, v140
	v_pk_add_f16 v65, v185, v141
	ds_read_b64_tr_b16 v[172:173], v184 offset:28672
	ds_read_b64_tr_b16 v[174:175], v184 offset:29184
	s_waitcnt lgkmcnt(10)
	v_mfma_f32_32x32x16_f16 v[80:95], v[168:171], v[136:139], v[32:47]
	v_exp_f32_e32 v71, v71
	v_cvt_pk_f16_f32 v142, v68, v69
	v_cvt_pk_f16_f32 v143, v70, v71
	v_pk_add_f16 v64, v64, v142
	v_pk_add_f16 v65, v65, v143
	ds_read_b64_tr_b16 v[168:169], v184 offset:25600
	ds_read_b64_tr_b16 v[170:171], v184 offset:26112
	s_waitcnt lgkmcnt(11)
	v_mfma_f32_32x32x16_f16 v[96:111], v[164:167], v[128:131], v[96:111]
	v_exp_f32_e32 v75, v75
	v_cvt_pk_f16_f32 v132, v72, v73
	v_cvt_pk_f16_f32 v133, v74, v75
	v_pk_add_f16 v64, v64, v132
	v_pk_add_f16 v65, v65, v133
	ds_read_b64_tr_b16 v[72:73], v184 offset:29696
	ds_read_b64_tr_b16 v[74:75], v184 offset:30208
	s_waitcnt lgkmcnt(12)
	v_mfma_f32_32x32x16_f16 v[80:95], v[160:163], v[128:131], v[80:95]
	v_exp_f32_e32 v79, v79
	v_cvt_pk_f16_f32 v134, v76, v77
	v_cvt_pk_f16_f32 v135, v78, v79
	v_pk_add_f16 v64, v64, v134
	v_pk_add_f16 v65, v65, v135
	ds_read_b64_tr_b16 v[68:69], v184 offset:26624
	ds_read_b64_tr_b16 v[70:71], v184 offset:27136
	s_waitcnt lgkmcnt(13)
	v_mfma_f32_32x32x16_f16 v[96:111], v[156:159], v[120:123], v[96:111]
	v_exp_f32_e32 v51, v51
	v_cvt_pk_f16_f32 v124, v48, v49
	v_cvt_pk_f16_f32 v125, v50, v51
	v_pk_add_f16 v48, v64, v124
	v_pk_add_f16 v49, v65, v125
	ds_read_b64_tr_b16 v[64:65], v184 offset:30720
	ds_read_b64_tr_b16 v[66:67], v184 offset:31232
	s_waitcnt lgkmcnt(14)
	v_mfma_f32_32x32x16_f16 v[80:95], v[152:155], v[120:123], v[80:95]
	v_exp_f32_e32 v55, v55
	v_cvt_pk_f16_f32 v126, v52, v53
	v_cvt_pk_f16_f32 v127, v54, v55
	v_pk_add_f16 v48, v48, v126
	v_pk_add_f16 v49, v49, v127
	ds_read_b64_tr_b16 v[52:53], v184 offset:27648
	ds_read_b64_tr_b16 v[54:55], v184 offset:28160
	s_waitcnt lgkmcnt(14)
	v_mfma_f32_32x32x16_f16 v[96:111], v[148:151], v[116:119], v[96:111]
	v_exp_f32_e32 v59, v59
	v_cvt_pk_f16_f32 v112, v56, v57
	v_cvt_pk_f16_f32 v113, v58, v59
	v_pk_add_f16 v56, v48, v112
	v_pk_add_f16 v57, v49, v113
	ds_read_b64_tr_b16 v[48:49], v184 offset:31744
	ds_read_b64_tr_b16 v[50:51], v184 offset:32256
	v_mfma_f32_32x32x16_f16 v[80:95], v[144:147], v[116:119], v[80:95]
	v_exp_f32_e32 v63, v63
	v_cvt_pk_f16_f32 v114, v60, v61
	v_cvt_pk_f16_f32 v115, v62, v63
	v_pk_add_f16 v56, v56, v114
	v_pk_add_f16 v57, v57, v115
	v_pk_add_f16 v56, v56, v57
	s_cmp_lt_u32 s26, 4
	s_cbranch_scc1 .Latt_pr_1
	s_setprio 1
.Latt_pr_1:
	s_add_i32 s9, s23, s30
	v_cvt_f32_f16_e32 v58, v56
	v_cvt_f32_f16_sdwa v59, v56 dst_sel:DWORD dst_unused:UNUSED_PAD src0_sel:WORD_1
	v_add_f32_e32 v58, v59, v58
	v_add_f32_e32 v184, v199, v58
	v_lshl_add_u64 v[56:57], v[188:189], 0, s[4:5]
	s_mov_b32 m0, s9
	s_nop 0
	global_load_lds_dwordx4 v[56:57], off
	v_lshl_add_u64 v[56:57], v[188:189], 0, s[10:11]
	s_add_i32 s9, s21, s31
	s_mov_b32 m0, s9
	s_nop 0
	global_load_lds_dwordx4 v[56:57], off
	s_waitcnt lgkmcnt(14)
	v_mfma_f32_32x32x16_f16 v[0:15], v[140:143], v[176:179], v[0:15]
	v_max_f32_e32 v202, v97, v97
	v_max_f32_e32 v203, v96, v96
	v_max_f32_e32 v202, v203, v202
	v_max3_f32 v203, v98, v99, v81
	v_max3_f32 v202, v202, v80, v82
	v_max3_f32 v202, v202, v83, v100
	v_max3_f32 v203, v203, v102, v103
	v_max3_f32 v202, v202, v101, v84
	s_waitcnt lgkmcnt(12)
	v_mfma_f32_32x32x16_f16 v[16:31], v[140:143], v[172:175], v[16:31]
	v_max3_f32 v203, v203, v86, v87
	v_max3_f32 v202, v202, v85, v104
	v_max3_f32 v203, v203, v106, v107
	v_max3_f32 v202, v202, v105, v88
	v_max3_f32 v203, v203, v90, v91
	v_max3_f32 v202, v202, v89, v108
	v_max3_f32 v203, v203, v110, v111
	v_max3_f32 v202, v202, v109, v92
	v_add_u32_e32 v60, s21, v198
	ds_read_b128 v[56:59], v60
	ds_read_b128 v[144:147], v60 offset:512
	s_waitcnt lgkmcnt(12)
	v_mfma_f32_32x32x16_f16 v[0:15], v[132:135], v[168:171], v[0:15]
	v_max3_f32 v203, v203, v94, v95
	v_max3_f32 v202, v202, v93, v203
	v_mov_b32_e32 v203, v202
	s_nop 1
	v_permlane32_swap_b32_e32 v202, v203
	v_max_f32_e32 v203, v203, v203
	v_max_f32_e32 v202, v202, v202
	v_max_f32_e32 v202, v202, v203
	v_cmp_lt_f32_e32 vcc, s22, v202
	s_nop 1
	s_cmp_lg_u64 vcc, 0
	s_cselect_b64 s[16:17], -1, 0
	s_nop 0
	s_cbranch_vccnz .LBB3_9
.LBB3_2:
	ds_read_b128 v[176:179], v60 offset:2048
	ds_read_b128 v[168:171], v60 offset:2560
	s_waitcnt lgkmcnt(12)
	v_mfma_f32_32x32x16_f16 v[16:31], v[132:135], v[72:75], v[16:31]
	v_exp_f32_e32 v96, v96
	v_exp_f32_e32 v97, v97
	v_exp_f32_e32 v98, v98
	v_exp_f32_e32 v100, v100
	v_exp_f32_e32 v101, v101
	ds_read_b128 v[172:175], v60 offset:4096
	ds_read_b128 v[160:163], v60 offset:4608
	s_waitcnt lgkmcnt(12)
	v_mfma_f32_32x32x16_f16 v[0:15], v[124:127], v[68:71], v[0:15]
	v_exp_f32_e32 v102, v102
	v_exp_f32_e32 v104, v104
	v_exp_f32_e32 v105, v105
	v_exp_f32_e32 v106, v106
	v_exp_f32_e32 v108, v108
	ds_read_b128 v[164:167], v60 offset:6144
	ds_read_b128 v[156:159], v60 offset:6656
	s_waitcnt lgkmcnt(12)
	v_mfma_f32_32x32x16_f16 v[16:31], v[124:127], v[64:67], v[16:31]
	v_exp_f32_e32 v109, v109
	v_exp_f32_e32 v110, v110
	v_exp_f32_e32 v80, v80
	v_exp_f32_e32 v81, v81
	v_exp_f32_e32 v82, v82
	s_waitcnt lgkmcnt(10)
	v_mfma_f32_32x32x16_f16 v[0:15], v[112:115], v[52:55], v[0:15]
	v_exp_f32_e32 v84, v84
	v_exp_f32_e32 v85, v85
	v_exp_f32_e32 v86, v86
	v_exp_f32_e32 v88, v88
	v_exp_f32_e32 v89, v89
	s_waitcnt lgkmcnt(8)
	v_mfma_f32_32x32x16_f16 v[16:31], v[112:115], v[48:51], v[16:31]
	v_exp_f32_e32 v90, v90
	v_exp_f32_e32 v92, v92
	v_exp_f32_e32 v93, v93
	v_exp_f32_e32 v94, v94
	s_waitcnt vmcnt(2) lgkmcnt(0)
	s_barrier
	s_setprio 0
	s_andn2_b64 vcc, exec, s[16:17]
	s_cbranch_vccnz .LBB3_4
	s_waitcnt lgkmcnt(0)
	v_add_u32_e32 v64, s29, v195
	ds_read_b128 v[48:51], v64 offset:49248
	ds_read_b128 v[52:55], v64 offset:49216
	ds_read_b128 v[60:63], v64 offset:49184
	ds_read_b128 v[64:67], v64 offset:49152
	s_waitcnt lgkmcnt(3)
	v_pk_mul_f32 v[12:13], v[12:13], v[48:49]
	s_waitcnt lgkmcnt(2)
	v_pk_mul_f32 v[8:9], v[8:9], v[52:53]
	s_waitcnt lgkmcnt(1)
	v_pk_mul_f32 v[4:5], v[4:5], v[60:61]
	v_pk_mul_f32 v[14:15], v[14:15], v[50:51]
	v_pk_mul_f32 v[10:11], v[10:11], v[54:55]
	v_pk_mul_f32 v[6:7], v[6:7], v[62:63]
	s_waitcnt lgkmcnt(0)
	v_pk_mul_f32 v[2:3], v[2:3], v[66:67]
	v_pk_mul_f32 v[0:1], v[0:1], v[64:65]
	v_pk_mul_f32 v[28:29], v[28:29], v[48:49]
	v_pk_mul_f32 v[24:25], v[24:25], v[52:53]
	v_pk_mul_f32 v[20:21], v[20:21], v[60:61]
	v_pk_mul_f32 v[30:31], v[30:31], v[50:51]
	v_pk_mul_f32 v[26:27], v[26:27], v[54:55]
	v_pk_mul_f32 v[22:23], v[22:23], v[62:63]
	v_pk_mul_f32 v[18:19], v[18:19], v[66:67]
	v_pk_mul_f32 v[16:17], v[16:17], v[64:65]
.LBB3_4:
	s_add_i32 s9, s21, 0x2000
	s_cmpk_lg_i32 s21, 0x4000
	s_cselect_b32 s24, s9, 0
	v_lshl_add_u64 v[200:201], v[188:189], 0, s[2:3]
	v_add_u32_e32 v199, s23, v194
	ds_read_b64_tr_b16 v[152:153], v199 offset:24576
	ds_read_b64_tr_b16 v[154:155], v199 offset:25088
	s_waitcnt lgkmcnt(9)
	v_mfma_f32_32x32x16_f16 v[64:79], v[56:59], v[136:139], v[32:47]
	v_exp_f32_e32 v99, v99
	v_cvt_pk_f16_f32 v140, v96, v97
	v_cvt_pk_f16_f32 v141, v98, v99
	v_pk_add_f16 v48, v185, v140
	v_pk_add_f16 v49, v185, v141
	ds_read_b64_tr_b16 v[148:149], v199 offset:28672
	ds_read_b64_tr_b16 v[150:151], v199 offset:29184
	v_exp_f32_e32 v103, v103
	v_cvt_pk_f16_f32 v142, v100, v101
	v_cvt_pk_f16_f32 v143, v102, v103
	v_pk_add_f16 v96, v48, v142
	v_pk_add_f16 v97, v49, v143
	s_waitcnt lgkmcnt(10)
	v_mfma_f32_32x32x16_f16 v[48:63], v[144:147], v[136:139], v[32:47]
	ds_read_b64_tr_b16 v[144:145], v199 offset:25600
	ds_read_b64_tr_b16 v[146:147], v199 offset:26112
	s_waitcnt lgkmcnt(11)
	v_mfma_f32_32x32x16_f16 v[64:79], v[176:179], v[128:131], v[64:79]
	v_exp_f32_e32 v107, v107
	v_cvt_pk_f16_f32 v132, v104, v105
	v_cvt_pk_f16_f32 v133, v106, v107
	v_pk_add_f16 v96, v96, v132
	v_pk_add_f16 v97, v97, v133
	ds_read_b64_tr_b16 v[104:105], v199 offset:29696
	ds_read_b64_tr_b16 v[106:107], v199 offset:30208
	s_waitcnt lgkmcnt(12)
	v_mfma_f32_32x32x16_f16 v[48:63], v[168:171], v[128:131], v[48:63]
	v_exp_f32_e32 v111, v111
	v_cvt_pk_f16_f32 v134, v108, v109
	v_cvt_pk_f16_f32 v135, v110, v111
	v_pk_add_f16 v96, v96, v134
	v_pk_add_f16 v97, v97, v135
	ds_read_b64_tr_b16 v[100:101], v199 offset:26624
	ds_read_b64_tr_b16 v[102:103], v199 offset:27136
	s_waitcnt lgkmcnt(13)
	v_mfma_f32_32x32x16_f16 v[64:79], v[172:175], v[120:123], v[64:79]
	v_exp_f32_e32 v83, v83
	v_cvt_pk_f16_f32 v124, v80, v81
	v_cvt_pk_f16_f32 v125, v82, v83
	v_pk_add_f16 v80, v96, v124
	v_pk_add_f16 v81, v97, v125
	ds_read_b64_tr_b16 v[96:97], v199 offset:30720
	ds_read_b64_tr_b16 v[98:99], v199 offset:31232
	s_waitcnt lgkmcnt(14)
	v_mfma_f32_32x32x16_f16 v[48:63], v[160:163], v[120:123], v[48:63]
	v_exp_f32_e32 v87, v87
	v_cvt_pk_f16_f32 v126, v84, v85
	v_cvt_pk_f16_f32 v127, v86, v87
	v_pk_add_f16 v80, v80, v126
	v_pk_add_f16 v81, v81, v127
	ds_read_b64_tr_b16 v[84:85], v199 offset:27648
	ds_read_b64_tr_b16 v[86:87], v199 offset:28160
	s_waitcnt lgkmcnt(14)
	v_mfma_f32_32x32x16_f16 v[64:79], v[164:167], v[116:119], v[64:79]
	v_exp_f32_e32 v91, v91
	v_cvt_pk_f16_f32 v112, v88, v89
	v_cvt_pk_f16_f32 v113, v90, v91
	v_pk_add_f16 v88, v80, v112
	v_pk_add_f16 v89, v81, v113
	ds_read_b64_tr_b16 v[80:81], v199 offset:31744
	ds_read_b64_tr_b16 v[82:83], v199 offset:32256
	v_mfma_f32_32x32x16_f16 v[48:63], v[156:159], v[116:119], v[48:63]
	v_exp_f32_e32 v95, v95
	v_cvt_pk_f16_f32 v114, v92, v93
	v_cvt_pk_f16_f32 v115, v94, v95
	v_pk_add_f16 v88, v88, v114
	v_pk_add_f16 v89, v89, v115
	v_pk_add_f16 v88, v88, v89
	s_cmp_lt_u32 s26, 4
	s_cbranch_scc1 .Latt_pr_2
	s_setprio 1
.Latt_pr_2:
	s_add_i32 s9, s21, s30
	v_cvt_f32_f16_e32 v90, v88
	v_cvt_f32_f16_sdwa v91, v88 dst_sel:DWORD dst_unused:UNUSED_PAD src0_sel:WORD_1
	v_add_f32_e32 v90, v91, v90
	v_add_f32_e32 v199, v184, v90
	v_lshl_add_u64 v[88:89], v[200:201], 0, s[12:13]
	s_mov_b32 m0, s9
	s_nop 0
	global_load_lds_dwordx4 v[88:89], off
	v_lshl_add_u64 v[188:189], v[188:189], 0, s[14:15]
	s_add_i32 s9, s24, s31
	s_mov_b32 m0, s9
	s_nop 0
	global_load_lds_dwordx4 v[188:189], off
	s_waitcnt lgkmcnt(14)
	v_mfma_f32_32x32x16_f16 v[0:15], v[140:143], v[152:155], v[0:15]
	v_max_f32_e32 v202, v65, v65
	v_max_f32_e32 v203, v64, v64
	v_max_f32_e32 v202, v203, v202
	v_max3_f32 v203, v66, v67, v49
	v_max3_f32 v202, v202, v48, v50
	v_max3_f32 v202, v202, v51, v68
	v_max3_f32 v203, v203, v70, v71
	v_max3_f32 v202, v202, v69, v52
	s_waitcnt lgkmcnt(12)
	v_mfma_f32_32x32x16_f16 v[16:31], v[140:143], v[148:151], v[16:31]
	v_max3_f32 v203, v203, v54, v55
	v_max3_f32 v202, v202, v53, v72
	v_max3_f32 v203, v203, v74, v75
	v_max3_f32 v202, v202, v73, v56
	v_max3_f32 v203, v203, v58, v59
	v_max3_f32 v202, v202, v57, v76
	v_max3_f32 v203, v203, v78, v79
	v_max3_f32 v202, v202, v77, v60
	v_add_u32_e32 v88, s24, v198
	ds_read_b128 v[172:175], v88
	ds_read_b128 v[168:171], v88 offset:512
	s_waitcnt lgkmcnt(12)
	v_mfma_f32_32x32x16_f16 v[0:15], v[132:135], v[144:147], v[0:15]
	v_max3_f32 v203, v203, v62, v63
	v_max3_f32 v202, v202, v61, v203
	v_mov_b32_e32 v203, v202
	s_nop 1
	v_permlane32_swap_b32_e32 v202, v203
	v_max_f32_e32 v203, v203, v203
	v_max_f32_e32 v202, v202, v202
	v_max_f32_e32 v202, v202, v203
	v_cmp_lt_f32_e32 vcc, s22, v202
	s_nop 1
	s_cmp_lg_u64 vcc, 0
	s_cselect_b64 s[16:17], -1, 0
	s_nop 0
	s_cbranch_vccnz .LBB3_12
.LBB3_5:
	ds_read_b128 v[164:167], v88 offset:2048
	ds_read_b128 v[160:163], v88 offset:2560
	s_waitcnt lgkmcnt(12)
	v_mfma_f32_32x32x16_f16 v[16:31], v[132:135], v[104:107], v[16:31]
	v_exp_f32_e32 v64, v64
	v_exp_f32_e32 v65, v65
	v_exp_f32_e32 v66, v66
	v_exp_f32_e32 v68, v68
	v_exp_f32_e32 v69, v69
	ds_read_b128 v[156:159], v88 offset:4096
	ds_read_b128 v[152:155], v88 offset:4608
	s_waitcnt lgkmcnt(12)
	v_mfma_f32_32x32x16_f16 v[0:15], v[124:127], v[100:103], v[0:15]
	v_exp_f32_e32 v70, v70
	v_exp_f32_e32 v72, v72
	v_exp_f32_e32 v73, v73
	v_exp_f32_e32 v74, v74
	v_exp_f32_e32 v76, v76
	ds_read_b128 v[148:151], v88 offset:6144
	ds_read_b128 v[144:147], v88 offset:6656
	s_waitcnt lgkmcnt(12)
	v_mfma_f32_32x32x16_f16 v[16:31], v[124:127], v[96:99], v[16:31]
	v_exp_f32_e32 v77, v77
	v_exp_f32_e32 v78, v78
	v_exp_f32_e32 v48, v48
	v_exp_f32_e32 v49, v49
	v_exp_f32_e32 v50, v50
	s_waitcnt lgkmcnt(10)
	v_mfma_f32_32x32x16_f16 v[0:15], v[112:115], v[84:87], v[0:15]
	v_exp_f32_e32 v52, v52
	v_exp_f32_e32 v53, v53
	v_exp_f32_e32 v54, v54
	v_exp_f32_e32 v56, v56
	v_exp_f32_e32 v57, v57
	s_waitcnt lgkmcnt(8)
	v_mfma_f32_32x32x16_f16 v[16:31], v[112:115], v[80:83], v[16:31]
	v_exp_f32_e32 v58, v58
	v_exp_f32_e32 v60, v60
	v_exp_f32_e32 v61, v61
	v_exp_f32_e32 v62, v62
	s_waitcnt vmcnt(2) lgkmcnt(0)
	s_barrier
	s_setprio 0
	s_andn2_b64 vcc, exec, s[16:17]
	s_cbranch_vccnz .LBB3_7
	s_waitcnt lgkmcnt(0)
	v_add_u32_e32 v92, s29, v195
	ds_read_b128 v[80:83], v92 offset:49248
	ds_read_b128 v[84:87], v92 offset:49216
	ds_read_b128 v[88:91], v92 offset:49152
	ds_read_b128 v[92:95], v92 offset:49184
	s_waitcnt lgkmcnt(3)
	v_pk_mul_f32 v[14:15], v[14:15], v[82:83]
	v_pk_mul_f32 v[12:13], v[12:13], v[80:81]
	s_waitcnt lgkmcnt(2)
	v_pk_mul_f32 v[10:11], v[10:11], v[86:87]
	v_pk_mul_f32 v[8:9], v[8:9], v[84:85]
	s_waitcnt lgkmcnt(0)
	v_pk_mul_f32 v[6:7], v[6:7], v[94:95]
	v_pk_mul_f32 v[4:5], v[4:5], v[92:93]
	v_pk_mul_f32 v[2:3], v[2:3], v[90:91]
	v_pk_mul_f32 v[0:1], v[0:1], v[88:89]
	v_pk_mul_f32 v[30:31], v[30:31], v[82:83]
	v_pk_mul_f32 v[28:29], v[28:29], v[80:81]
	v_pk_mul_f32 v[26:27], v[26:27], v[86:87]
	v_pk_mul_f32 v[24:25], v[24:25], v[84:85]
	v_pk_mul_f32 v[22:23], v[22:23], v[94:95]
	v_pk_mul_f32 v[20:21], v[20:21], v[92:93]
	v_pk_mul_f32 v[18:19], v[18:19], v[90:91]
	v_pk_mul_f32 v[16:17], v[16:17], v[88:89]

.LBB3_9:
	v_max_f32_e32 v32, v202, v202
	v_max_f32_e32 v202, 0, v32
	v_exp_f32_e64 v203, -v202
	v_add_f32_e32 v197, v197, v202
	v_xor_b32_e32 v32, 0x80000000, v197
	v_mov_b32_e32 v33, v32
	v_mov_b32_e32 v34, v32
	v_mov_b32_e32 v35, v32
	v_mov_b32_e32 v36, v32
	v_mov_b32_e32 v37, v32
	v_mov_b32_e32 v38, v32
	v_mov_b32_e32 v39, v32
	v_mov_b32_e32 v40, v32
	v_mov_b32_e32 v41, v32
	v_mov_b32_e32 v42, v32
	v_mov_b32_e32 v43, v32
	v_mov_b32_e32 v44, v32
	v_mov_b32_e32 v45, v32
	v_mov_b32_e32 v46, v32
	v_mov_b32_e32 v47, v32
	s_and_saveexec_b64 s[18:19], s[0:1]
	ds_write_b32 v196, v203 offset:49152
	s_or_b64 exec, exec, s[18:19]
	v_sub_f32_e32 v111, v111, v202
	v_sub_f32_e32 v110, v110, v202
	v_sub_f32_e32 v109, v109, v202
	v_sub_f32_e32 v108, v108, v202
	v_sub_f32_e32 v107, v107, v202
	v_sub_f32_e32 v106, v106, v202
	v_sub_f32_e32 v105, v105, v202
	v_sub_f32_e32 v104, v104, v202
	v_sub_f32_e32 v103, v103, v202
	v_sub_f32_e32 v102, v102, v202
	v_sub_f32_e32 v101, v101, v202
	v_sub_f32_e32 v100, v100, v202
	v_sub_f32_e32 v99, v99, v202
	v_sub_f32_e32 v98, v98, v202
	v_sub_f32_e32 v97, v97, v202
	v_sub_f32_e32 v96, v96, v202
	v_sub_f32_e32 v95, v95, v202
	v_sub_f32_e32 v94, v94, v202
	v_sub_f32_e32 v93, v93, v202
	v_sub_f32_e32 v92, v92, v202
	v_sub_f32_e32 v91, v91, v202
	v_sub_f32_e32 v90, v90, v202
	v_sub_f32_e32 v89, v89, v202
	v_sub_f32_e32 v88, v88, v202
	v_sub_f32_e32 v87, v87, v202
	v_sub_f32_e32 v86, v86, v202
	v_sub_f32_e32 v85, v85, v202
	v_sub_f32_e32 v84, v84, v202
	v_sub_f32_e32 v83, v83, v202
	v_sub_f32_e32 v82, v82, v202
	v_sub_f32_e32 v81, v81, v202
	v_sub_f32_e32 v80, v80, v202
	v_mul_f32_e32 v184, v184, v203
	s_branch .LBB3_2
.LBB3_12:
	v_max_f32_e32 v32, v202, v202
	v_max_f32_e32 v202, 0, v32
	v_exp_f32_e64 v203, -v202
	v_add_f32_e32 v197, v197, v202
	v_xor_b32_e32 v32, 0x80000000, v197
	v_mov_b32_e32 v33, v32
	v_mov_b32_e32 v34, v32
	v_mov_b32_e32 v35, v32
	v_mov_b32_e32 v36, v32
	v_mov_b32_e32 v37, v32
	v_mov_b32_e32 v38, v32
	v_mov_b32_e32 v39, v32
	v_mov_b32_e32 v40, v32
	v_mov_b32_e32 v41, v32
	v_mov_b32_e32 v42, v32
	v_mov_b32_e32 v43, v32
	v_mov_b32_e32 v44, v32
	v_mov_b32_e32 v45, v32
	v_mov_b32_e32 v46, v32
	v_mov_b32_e32 v47, v32
	s_and_saveexec_b64 s[18:19], s[0:1]
	ds_write_b32 v196, v203 offset:49152
	s_or_b64 exec, exec, s[18:19]
	v_sub_f32_e32 v79, v79, v202
	v_sub_f32_e32 v78, v78, v202
	v_sub_f32_e32 v77, v77, v202
	v_sub_f32_e32 v76, v76, v202
	v_sub_f32_e32 v75, v75, v202
	v_sub_f32_e32 v74, v74, v202
	v_sub_f32_e32 v73, v73, v202
	v_sub_f32_e32 v72, v72, v202
	v_sub_f32_e32 v71, v71, v202
	v_sub_f32_e32 v70, v70, v202
	v_sub_f32_e32 v69, v69, v202
	v_sub_f32_e32 v68, v68, v202
	v_sub_f32_e32 v67, v67, v202
	v_sub_f32_e32 v66, v66, v202
	v_sub_f32_e32 v65, v65, v202
	v_sub_f32_e32 v64, v64, v202
	v_sub_f32_e32 v63, v63, v202
	v_sub_f32_e32 v62, v62, v202
	v_sub_f32_e32 v61, v61, v202
	v_sub_f32_e32 v60, v60, v202
	v_sub_f32_e32 v59, v59, v202
	v_sub_f32_e32 v58, v58, v202
	v_sub_f32_e32 v57, v57, v202
	v_sub_f32_e32 v56, v56, v202
	v_sub_f32_e32 v55, v55, v202
	v_sub_f32_e32 v54, v54, v202
	v_sub_f32_e32 v53, v53, v202
	v_sub_f32_e32 v52, v52, v202
	v_sub_f32_e32 v51, v51, v202
	v_sub_f32_e32 v50, v50, v202
	v_sub_f32_e32 v49, v49, v202
	v_sub_f32_e32 v48, v48, v202
	v_mul_f32_e32 v199, v199, v203
	s_branch .LBB3_5
.LBB3_15:
	v_exp_f32_e32 v67, v67
	v_exp_f32_e32 v71, v71
	v_exp_f32_e32 v75, v75
	v_exp_f32_e32 v79, v79
	v_exp_f32_e32 v51, v51
	v_exp_f32_e32 v55, v55
	v_exp_f32_e32 v59, v59
	v_exp_f32_e32 v63, v63
	s_mov_b64 s[2:3], 0x836000
	v_lshl_add_u64 v[184:185], v[186:187], 0, s[2:3]
	s_mov_b32 s9, 27
	s_movk_i32 s33, 0x2000
	s_mov_b32 s3, 0
	s_movk_i32 s2, 0x4000
	s_mov_b64 s[4:5], 0x1b000
	v_mov_b32_e32 v188, 0
	s_mov_b64 s[10:11], 0x6000
	s_mov_b64 s[12:13], 0x2000
	s_mov_b32 s34, 0x41000000
	s_mov_b64 s[14:15], 0x8000
	s_mov_b64 s[16:17], 0x4000
	s_mov_b32 s35, 0

	.amdhsa_kernel _ZN3att8attn_fwdEPKDF16_PDF16_
		.amdhsa_group_segment_fixed_size 0
		.amdhsa_private_segment_fixed_size 0
		.amdhsa_kernarg_size 16
		.amdhsa_user_sgpr_count 2
		.amdhsa_user_sgpr_dispatch_ptr 0
		.amdhsa_user_sgpr_queue_ptr 0
		.amdhsa_user_sgpr_kernarg_segment_ptr 1
		.amdhsa_user_sgpr_dispatch_id 0
		.amdhsa_user_sgpr_kernarg_preload_length 0
		.amdhsa_user_sgpr_kernarg_preload_offset 0
		.amdhsa_user_sgpr_private_segment_size 0
		.amdhsa_uses_dynamic_stack 0
		.amdhsa_enable_private_segment 0
		.amdhsa_system_sgpr_workgroup_id_x 1
		.amdhsa_system_sgpr_workgroup_id_y 0
		.amdhsa_system_sgpr_workgroup_id_z 0
		.amdhsa_system_sgpr_workgroup_info 0
		.amdhsa_system_vgpr_workitem_id 0
		.amdhsa_next_free_vgpr 204
		.amdhsa_next_free_sgpr 36
		.amdhsa_accum_offset 204
		.amdhsa_reserve_vcc 1
		.amdhsa_float_round_mode_32 0
		.amdhsa_float_round_mode_16_64 0
		.amdhsa_float_denorm_mode_32 3
		.amdhsa_float_denorm_mode_16_64 3
		.amdhsa_dx10_clamp 1
		.amdhsa_ieee_mode 1
		.amdhsa_fp16_overflow 0
		.amdhsa_tg_split 0
		.amdhsa_exception_fp_ieee_invalid_op 0
		.amdhsa_exception_fp_denorm_src 0
		.amdhsa_exception_fp_ieee_div_zero 0
		.amdhsa_exception_fp_ieee_overflow 0
		.amdhsa_exception_fp_ieee_underflow 0
		.amdhsa_exception_fp_ieee_inexact 0
		.amdhsa_exception_int_div_zero 0
	.end_amdhsa_kernel

amdhsa.kernels:
  - .agpr_count:     0
    .args:
      - .actual_access:  read_only
        .address_space:  global
        .offset:         0
        .size:           8
        .value_kind:     global_buffer
      - .actual_access:  read_only
        .address_space:  global
        .offset:         8
        .size:           8
        .value_kind:     global_buffer
      - .actual_access:  read_only
        .address_space:  global
        .offset:         16
        .size:           8
        .value_kind:     global_buffer
      - .actual_access:  read_only
        .address_space:  global
        .offset:         24
        .size:           8
        .value_kind:     global_buffer
      - .actual_access:  read_only
        .address_space:  global
        .offset:         32
        .size:           8
        .value_kind:     global_buffer
      - .actual_access:  write_only
        .address_space:  global
        .offset:         40
        .size:           8
        .value_kind:     global_buffer
      - .actual_access:  read_only
        .address_space:  global
        .offset:         48
        .size:           8
        .value_kind:     global_buffer
      - .actual_access:  read_only
        .address_space:  global
        .offset:         56
        .size:           8
        .value_kind:     global_buffer
      - .actual_access:  read_only
        .address_space:  global
        .offset:         64
        .size:           8
        .value_kind:     global_buffer
      - .actual_access:  write_only
        .address_space:  global
        .offset:         72
        .size:           8
        .value_kind:     global_buffer
    .group_segment_fixed_size: 0
    .kernarg_segment_align: 8
    .kernarg_segment_size: 80
    .language:       OpenCL C
    .language_version:
      - 2
      - 0
    .max_flat_workgroup_size: 256
    .name:           _Z7cvt_allPKfS0_S0_S0_S0_PDF16_S0_S0_S0_Pf
    .private_segment_fixed_size: 0
    .sgpr_count:     16
    .sgpr_spill_count: 0
    .symbol:         _Z7cvt_allPKfS0_S0_S0_S0_PDF16_S0_S0_S0_Pf.kd
    .uniform_work_group_size: 1
    .uses_dynamic_stack: false
    .vgpr_count:     22
    .vgpr_spill_count: 0
    .wavefront_size: 64
  - .agpr_count:     0
    .args:
      - .address_space:  global
        .offset:         0
        .size:           8
        .value_kind:     global_buffer
      - .address_space:  global
        .offset:         8
        .size:           8
        .value_kind:     global_buffer
      - .actual_access:  read_only
        .address_space:  global
        .offset:         16
        .size:           8
        .value_kind:     global_buffer
      - .actual_access:  write_only
        .address_space:  global
        .offset:         24
        .size:           8
        .value_kind:     global_buffer
      - .offset:         32
        .size:           4
        .value_kind:     hidden_block_count_x
      - .offset:         36
        .size:           4
        .value_kind:     hidden_block_count_y
      - .offset:         40
        .size:           4
        .value_kind:     hidden_block_count_z
      - .offset:         44
        .size:           2
        .value_kind:     hidden_group_size_x
      - .offset:         46
        .size:           2
        .value_kind:     hidden_group_size_y
      - .offset:         48
        .size:           2
        .value_kind:     hidden_group_size_z
      - .offset:         50
        .size:           2
        .value_kind:     hidden_remainder_x
      - .offset:         52
        .size:           2
        .value_kind:     hidden_remainder_y
      - .offset:         54
        .size:           2
        .value_kind:     hidden_remainder_z
      - .offset:         72
        .size:           8
        .value_kind:     hidden_global_offset_x
      - .offset:         80
        .size:           8
        .value_kind:     hidden_global_offset_y
      - .offset:         88
        .size:           8
        .value_kind:     hidden_global_offset_z
      - .offset:         96
        .size:           2
        .value_kind:     hidden_grid_dims
      - .offset:         152
        .size:           4
        .value_kind:     hidden_dynamic_lds_size
    .group_segment_fixed_size: 0
    .kernarg_segment_align: 8
    .kernarg_segment_size: 288
    .language:       OpenCL C
    .language_version:
      - 2
      - 0
    .max_flat_workgroup_size: 512
    .name:           _ZN6g128w88gemm_outEPKDF16_S1_PKfPf
    .private_segment_fixed_size: 0
    .sgpr_count:     29
    .sgpr_spill_count: 0
    .symbol:         _ZN6g128w88gemm_outEPKDF16_S1_PKfPf.kd
    .uniform_work_group_size: 1
    .uses_dynamic_stack: false
    .vgpr_count:     116
    .vgpr_spill_count: 0
    .wavefront_size: 64
  - .agpr_count:     0
    .args:
      - .address_space:  global
        .offset:         0
        .size:           8
        .value_kind:     global_buffer
      - .address_space:  global
        .offset:         8
        .size:           8
        .value_kind:     global_buffer
      - .actual_access:  read_only
        .address_space:  global
        .offset:         16
        .size:           8
        .value_kind:     global_buffer
      - .actual_access:  write_only
        .address_space:  global
        .offset:         24
        .size:           8
        .value_kind:     global_buffer
    .group_segment_fixed_size: 0
    .kernarg_segment_align: 8
    .kernarg_segment_size: 32
    .language:       OpenCL C
    .language_version:
      - 2
      - 0
    .max_flat_workgroup_size: 512
    .name:           _ZN4g2568gemm_qkvEPKDF16_S1_PKfPDF16_
    .private_segment_fixed_size: 0
    .sgpr_count:     50
    .sgpr_spill_count: 0
    .symbol:         _ZN4g2568gemm_qkvEPKDF16_S1_PKfPDF16_.kd
    .uniform_work_group_size: 1
    .uses_dynamic_stack: false
    .vgpr_count:     188
    .vgpr_spill_count: 0
    .wavefront_size: 64
  - .agpr_count:     0
    .args:
      - .address_space:  global
        .offset:         0
        .size:           8
        .value_kind:     global_buffer
      - .actual_access:  write_only
        .address_space:  global
        .offset:         8
        .size:           8
        .value_kind:     global_buffer
    .group_segment_fixed_size: 0
    .kernarg_segment_align: 8
    .kernarg_segment_size: 16
    .language:       OpenCL C
    .language_version:
      - 2
      - 0
    .max_flat_workgroup_size: 512
    .name:           _ZN3att8attn_fwdEPKDF16_PDF16_
    .private_segment_fixed_size: 0
    .sgpr_count:     42
    .sgpr_spill_count: 0
    .symbol:         _ZN3att8attn_fwdEPKDF16_PDF16_.kd
    .uniform_work_group_size: 1
    .uses_dynamic_stack: false
    .vgpr_count:     204
    .vgpr_spill_count: 0
    .wavefront_size: 64
